# g5: g4 + P5 fp8-image tail de-serialised (norm weights hoisted, next row loaded while current row converts, counted vmcnt)
# speedup vs baseline: 1.0031x; 1.0031x over previous
.LBB0_465:
	s_or_b64 exec, exec, s[10:11]
	s_ashr_i32 s95, s94, 31
	s_ashr_i32 s89, s88, 31
	global_load_dwordx4 v[200:203], v[50:51], off
	global_load_dwordx4 v[204:207], v[50:51], off offset:1024
	global_load_dwordx4 v[208:211], v[50:51], off offset:2048
	global_load_dwordx4 v[212:215], v[50:51], off offset:3072
	global_load_dwordx4 v[216:219], v[54:55], off
	global_load_dwordx4 v[220:223], v[56:57], off
	global_load_dwordx4 v[224:227], v[58:59], off
	global_load_dwordx4 v[228:231], v[60:61], off
	s_mov_b64 s[10:11], s[94:95]
	s_lshl_b64 s[10:11], s[10:11], 12
	v_lshl_add_u64 v[6:7], v[48:49], 0, s[10:11]
	global_load_dwordx2 v[232:233], v[6:7], off
	global_load_dwordx2 v[234:235], v[6:7], off offset:512
	global_load_dwordx2 v[236:237], v[6:7], off offset:1024
	global_load_dwordx2 v[238:239], v[6:7], off offset:1536
	global_load_dwordx2 v[240:241], v[6:7], off offset:2048
	global_load_dwordx2 v[242:243], v[6:7], off offset:2560
	global_load_dwordx2 v[244:245], v[6:7], off offset:3072
	global_load_dwordx2 v[246:247], v[6:7], off offset:3584
	s_add_i32 s10, s88, -6
	s_ashr_i32 s11, s10, 31
	s_lshl_b64 s[10:11], s[10:11], 12
	v_lshl_add_u64 v[6:7], v[48:49], 0, s[10:11]
	global_load_dwordx2 v[170:171], v[6:7], off
	global_load_dwordx2 v[172:173], v[6:7], off offset:512
	global_load_dwordx2 v[174:175], v[6:7], off offset:1024
	global_load_dwordx2 v[176:177], v[6:7], off offset:1536
	global_load_dwordx2 v[178:179], v[6:7], off offset:2048
	global_load_dwordx2 v[180:181], v[6:7], off offset:2560
	global_load_dwordx2 v[182:183], v[6:7], off offset:3072
	global_load_dwordx2 v[184:185], v[6:7], off offset:3584
	s_mov_b64 s[12:13], s[94:95]
	s_lshl_b64 s[12:13], s[12:13], 11
	v_lshl_add_u64 v[8:9], v[52:53], 0, s[12:13]
	s_waitcnt vmcnt(8)
	v_lshlrev_b32_e32 v2, 16, v232
	v_and_b32_e32 v3, 0xffff0000, v232
	v_mul_f32_e32 v2, v69, v2
	v_mul_f32_e32 v3, v69, v3
	v_mul_f32_e32 v2, v200, v2
	v_mul_f32_e32 v3, v201, v3
	v_cvt_pk_fp8_f32 v10, v2, v3
	v_lshlrev_b32_e32 v4, 16, v233
	v_and_b32_e32 v5, 0xffff0000, v233
	v_mul_f32_e32 v4, v69, v4
	v_mul_f32_e32 v5, v69, v5
	v_mul_f32_e32 v4, v202, v4
	v_mul_f32_e32 v5, v203, v5
	v_cvt_pk_fp8_f32 v10, v4, v5 op_sel:[0,0,1]
	global_store_dword v[8:9], v10, off
	v_lshlrev_b32_e32 v2, 16, v234
	v_and_b32_e32 v3, 0xffff0000, v234
	v_mul_f32_e32 v2, v69, v2
	v_mul_f32_e32 v3, v69, v3
	v_mul_f32_e32 v2, v204, v2
	v_mul_f32_e32 v3, v205, v3
	v_cvt_pk_fp8_f32 v12, v2, v3
	v_lshlrev_b32_e32 v4, 16, v235
	v_and_b32_e32 v5, 0xffff0000, v235
	v_mul_f32_e32 v4, v69, v4
	v_mul_f32_e32 v5, v69, v5
	v_mul_f32_e32 v4, v206, v4
	v_mul_f32_e32 v5, v207, v5
	v_cvt_pk_fp8_f32 v12, v4, v5 op_sel:[0,0,1]
	global_store_dword v[8:9], v12, off offset:256
	v_lshlrev_b32_e32 v2, 16, v236
	v_and_b32_e32 v3, 0xffff0000, v236
	v_mul_f32_e32 v2, v69, v2
	v_mul_f32_e32 v3, v69, v3
	v_mul_f32_e32 v2, v208, v2
	v_mul_f32_e32 v3, v209, v3
	v_cvt_pk_fp8_f32 v10, v2, v3
	v_lshlrev_b32_e32 v4, 16, v237
	v_and_b32_e32 v5, 0xffff0000, v237
	v_mul_f32_e32 v4, v69, v4
	v_mul_f32_e32 v5, v69, v5
	v_mul_f32_e32 v4, v210, v4
	v_mul_f32_e32 v5, v211, v5
	v_cvt_pk_fp8_f32 v10, v4, v5 op_sel:[0,0,1]
	global_store_dword v[8:9], v10, off offset:512
	v_lshlrev_b32_e32 v2, 16, v238
	v_and_b32_e32 v3, 0xffff0000, v238
	v_mul_f32_e32 v2, v69, v2
	v_mul_f32_e32 v3, v69, v3
	v_mul_f32_e32 v2, v212, v2
	v_mul_f32_e32 v3, v213, v3
	v_cvt_pk_fp8_f32 v12, v2, v3
	v_lshlrev_b32_e32 v4, 16, v239
	v_and_b32_e32 v5, 0xffff0000, v239
	v_mul_f32_e32 v4, v69, v4
	v_mul_f32_e32 v5, v69, v5
	v_mul_f32_e32 v4, v214, v4
	v_mul_f32_e32 v5, v215, v5
	v_cvt_pk_fp8_f32 v12, v4, v5 op_sel:[0,0,1]
	global_store_dword v[8:9], v12, off offset:768
	v_lshlrev_b32_e32 v2, 16, v240
	v_and_b32_e32 v3, 0xffff0000, v240
	v_mul_f32_e32 v2, v69, v2
	v_mul_f32_e32 v3, v69, v3
	v_mul_f32_e32 v2, v216, v2
	v_mul_f32_e32 v3, v217, v3
	v_cvt_pk_fp8_f32 v10, v2, v3
	v_lshlrev_b32_e32 v4, 16, v241
	v_and_b32_e32 v5, 0xffff0000, v241
	v_mul_f32_e32 v4, v69, v4
	v_mul_f32_e32 v5, v69, v5
	v_mul_f32_e32 v4, v218, v4
	v_mul_f32_e32 v5, v219, v5
	v_cvt_pk_fp8_f32 v10, v4, v5 op_sel:[0,0,1]
	global_store_dword v[8:9], v10, off offset:1024
	v_lshlrev_b32_e32 v2, 16, v242
	v_and_b32_e32 v3, 0xffff0000, v242
	v_mul_f32_e32 v2, v69, v2
	v_mul_f32_e32 v3, v69, v3
	v_mul_f32_e32 v2, v220, v2
	v_mul_f32_e32 v3, v221, v3
	v_cvt_pk_fp8_f32 v12, v2, v3
	v_lshlrev_b32_e32 v4, 16, v243
	v_and_b32_e32 v5, 0xffff0000, v243
	v_mul_f32_e32 v4, v69, v4
	v_mul_f32_e32 v5, v69, v5
	v_mul_f32_e32 v4, v222, v4
	v_mul_f32_e32 v5, v223, v5
	v_cvt_pk_fp8_f32 v12, v4, v5 op_sel:[0,0,1]
	global_store_dword v[8:9], v12, off offset:1280
	v_lshlrev_b32_e32 v2, 16, v244
	v_and_b32_e32 v3, 0xffff0000, v244
	v_mul_f32_e32 v2, v69, v2
	v_mul_f32_e32 v3, v69, v3
	v_mul_f32_e32 v2, v224, v2
	v_mul_f32_e32 v3, v225, v3
	v_cvt_pk_fp8_f32 v10, v2, v3
	v_lshlrev_b32_e32 v4, 16, v245
	v_and_b32_e32 v5, 0xffff0000, v245
	v_mul_f32_e32 v4, v69, v4
	v_mul_f32_e32 v5, v69, v5
	v_mul_f32_e32 v4, v226, v4
	v_mul_f32_e32 v5, v227, v5
	v_cvt_pk_fp8_f32 v10, v4, v5 op_sel:[0,0,1]
	global_store_dword v[8:9], v10, off offset:1536
	v_lshlrev_b32_e32 v2, 16, v246
	v_and_b32_e32 v3, 0xffff0000, v246
	v_mul_f32_e32 v2, v69, v2
	v_mul_f32_e32 v3, v69, v3
	v_mul_f32_e32 v2, v228, v2
	v_mul_f32_e32 v3, v229, v3
	v_cvt_pk_fp8_f32 v12, v2, v3
	v_lshlrev_b32_e32 v4, 16, v247
	v_and_b32_e32 v5, 0xffff0000, v247
	v_mul_f32_e32 v4, v69, v4
	v_mul_f32_e32 v5, v69, v5
	v_mul_f32_e32 v4, v230, v4
	v_mul_f32_e32 v5, v231, v5
	v_cvt_pk_fp8_f32 v12, v4, v5 op_sel:[0,0,1]
	global_store_dword v[8:9], v12, off offset:1792
	s_add_i32 s10, s88, -5
	s_ashr_i32 s11, s10, 31
	s_lshl_b64 s[10:11], s[10:11], 12
	v_lshl_add_u64 v[6:7], v[48:49], 0, s[10:11]
	global_load_dwordx2 v[232:233], v[6:7], off
	global_load_dwordx2 v[234:235], v[6:7], off offset:512
	global_load_dwordx2 v[236:237], v[6:7], off offset:1024
	global_load_dwordx2 v[238:239], v[6:7], off offset:1536
	global_load_dwordx2 v[240:241], v[6:7], off offset:2048
	global_load_dwordx2 v[242:243], v[6:7], off offset:2560
	global_load_dwordx2 v[244:245], v[6:7], off offset:3072
	global_load_dwordx2 v[246:247], v[6:7], off offset:3584
	s_add_i32 s12, s88, -6
	s_ashr_i32 s13, s12, 31
	s_lshl_b64 s[12:13], s[12:13], 11
	v_lshl_add_u64 v[8:9], v[52:53], 0, s[12:13]
	s_waitcnt vmcnt(16)
	v_lshlrev_b32_e32 v2, 16, v170
	v_and_b32_e32 v3, 0xffff0000, v170
	v_mul_f32_e32 v2, v68, v2
	v_mul_f32_e32 v3, v68, v3
	v_mul_f32_e32 v2, v200, v2
	v_mul_f32_e32 v3, v201, v3
	v_cvt_pk_fp8_f32 v10, v2, v3
	v_lshlrev_b32_e32 v4, 16, v171
	v_and_b32_e32 v5, 0xffff0000, v171
	v_mul_f32_e32 v4, v68, v4
	v_mul_f32_e32 v5, v68, v5
	v_mul_f32_e32 v4, v202, v4
	v_mul_f32_e32 v5, v203, v5
	v_cvt_pk_fp8_f32 v10, v4, v5 op_sel:[0,0,1]
	global_store_dword v[8:9], v10, off
	v_lshlrev_b32_e32 v2, 16, v172
	v_and_b32_e32 v3, 0xffff0000, v172
	v_mul_f32_e32 v2, v68, v2
	v_mul_f32_e32 v3, v68, v3
	v_mul_f32_e32 v2, v204, v2
	v_mul_f32_e32 v3, v205, v3
	v_cvt_pk_fp8_f32 v12, v2, v3
	v_lshlrev_b32_e32 v4, 16, v173
	v_and_b32_e32 v5, 0xffff0000, v173
	v_mul_f32_e32 v4, v68, v4
	v_mul_f32_e32 v5, v68, v5
	v_mul_f32_e32 v4, v206, v4
	v_mul_f32_e32 v5, v207, v5
	v_cvt_pk_fp8_f32 v12, v4, v5 op_sel:[0,0,1]
	global_store_dword v[8:9], v12, off offset:256
	v_lshlrev_b32_e32 v2, 16, v174
	v_and_b32_e32 v3, 0xffff0000, v174
	v_mul_f32_e32 v2, v68, v2
	v_mul_f32_e32 v3, v68, v3
	v_mul_f32_e32 v2, v208, v2
	v_mul_f32_e32 v3, v209, v3
	v_cvt_pk_fp8_f32 v10, v2, v3
	v_lshlrev_b32_e32 v4, 16, v175
	v_and_b32_e32 v5, 0xffff0000, v175
	v_mul_f32_e32 v4, v68, v4
	v_mul_f32_e32 v5, v68, v5
	v_mul_f32_e32 v4, v210, v4
	v_mul_f32_e32 v5, v211, v5
	v_cvt_pk_fp8_f32 v10, v4, v5 op_sel:[0,0,1]
	global_store_dword v[8:9], v10, off offset:512
	v_lshlrev_b32_e32 v2, 16, v176
	v_and_b32_e32 v3, 0xffff0000, v176
	v_mul_f32_e32 v2, v68, v2
	v_mul_f32_e32 v3, v68, v3
	v_mul_f32_e32 v2, v212, v2
	v_mul_f32_e32 v3, v213, v3
	v_cvt_pk_fp8_f32 v12, v2, v3
	v_lshlrev_b32_e32 v4, 16, v177
	v_and_b32_e32 v5, 0xffff0000, v177
	v_mul_f32_e32 v4, v68, v4
	v_mul_f32_e32 v5, v68, v5
	v_mul_f32_e32 v4, v214, v4
	v_mul_f32_e32 v5, v215, v5
	v_cvt_pk_fp8_f32 v12, v4, v5 op_sel:[0,0,1]
	global_store_dword v[8:9], v12, off offset:768
	v_lshlrev_b32_e32 v2, 16, v178
	v_and_b32_e32 v3, 0xffff0000, v178
	v_mul_f32_e32 v2, v68, v2
	v_mul_f32_e32 v3, v68, v3
	v_mul_f32_e32 v2, v216, v2
	v_mul_f32_e32 v3, v217, v3
	v_cvt_pk_fp8_f32 v10, v2, v3
	v_lshlrev_b32_e32 v4, 16, v179
	v_and_b32_e32 v5, 0xffff0000, v179
	v_mul_f32_e32 v4, v68, v4
	v_mul_f32_e32 v5, v68, v5
	v_mul_f32_e32 v4, v218, v4
	v_mul_f32_e32 v5, v219, v5
	v_cvt_pk_fp8_f32 v10, v4, v5 op_sel:[0,0,1]
	global_store_dword v[8:9], v10, off offset:1024
	v_lshlrev_b32_e32 v2, 16, v180
	v_and_b32_e32 v3, 0xffff0000, v180
	v_mul_f32_e32 v2, v68, v2
	v_mul_f32_e32 v3, v68, v3
	v_mul_f32_e32 v2, v220, v2
	v_mul_f32_e32 v3, v221, v3
	v_cvt_pk_fp8_f32 v12, v2, v3
	v_lshlrev_b32_e32 v4, 16, v181
	v_and_b32_e32 v5, 0xffff0000, v181
	v_mul_f32_e32 v4, v68, v4
	v_mul_f32_e32 v5, v68, v5
	v_mul_f32_e32 v4, v222, v4
	v_mul_f32_e32 v5, v223, v5
	v_cvt_pk_fp8_f32 v12, v4, v5 op_sel:[0,0,1]
	global_store_dword v[8:9], v12, off offset:1280
	v_lshlrev_b32_e32 v2, 16, v182
	v_and_b32_e32 v3, 0xffff0000, v182
	v_mul_f32_e32 v2, v68, v2
	v_mul_f32_e32 v3, v68, v3
	v_mul_f32_e32 v2, v224, v2
	v_mul_f32_e32 v3, v225, v3
	v_cvt_pk_fp8_f32 v10, v2, v3
	v_lshlrev_b32_e32 v4, 16, v183
	v_and_b32_e32 v5, 0xffff0000, v183
	v_mul_f32_e32 v4, v68, v4
	v_mul_f32_e32 v5, v68, v5
	v_mul_f32_e32 v4, v226, v4
	v_mul_f32_e32 v5, v227, v5
	v_cvt_pk_fp8_f32 v10, v4, v5 op_sel:[0,0,1]
	global_store_dword v[8:9], v10, off offset:1536
	v_lshlrev_b32_e32 v2, 16, v184
	v_and_b32_e32 v3, 0xffff0000, v184
	v_mul_f32_e32 v2, v68, v2
	v_mul_f32_e32 v3, v68, v3
	v_mul_f32_e32 v2, v228, v2
	v_mul_f32_e32 v3, v229, v3
	v_cvt_pk_fp8_f32 v12, v2, v3
	v_lshlrev_b32_e32 v4, 16, v185
	v_and_b32_e32 v5, 0xffff0000, v185
	v_mul_f32_e32 v4, v68, v4
	v_mul_f32_e32 v5, v68, v5
	v_mul_f32_e32 v4, v230, v4
	v_mul_f32_e32 v5, v231, v5
	v_cvt_pk_fp8_f32 v12, v4, v5 op_sel:[0,0,1]
	global_store_dword v[8:9], v12, off offset:1792
	s_add_i32 s10, s88, -4
	s_ashr_i32 s11, s10, 31
	s_lshl_b64 s[10:11], s[10:11], 12
	v_lshl_add_u64 v[6:7], v[48:49], 0, s[10:11]
	global_load_dwordx2 v[170:171], v[6:7], off
	global_load_dwordx2 v[172:173], v[6:7], off offset:512
	global_load_dwordx2 v[174:175], v[6:7], off offset:1024
	global_load_dwordx2 v[176:177], v[6:7], off offset:1536
	global_load_dwordx2 v[178:179], v[6:7], off offset:2048
	global_load_dwordx2 v[180:181], v[6:7], off offset:2560
	global_load_dwordx2 v[182:183], v[6:7], off offset:3072
	global_load_dwordx2 v[184:185], v[6:7], off offset:3584
	s_add_i32 s12, s88, -5
	s_ashr_i32 s13, s12, 31
	s_lshl_b64 s[12:13], s[12:13], 11
	v_lshl_add_u64 v[8:9], v[52:53], 0, s[12:13]
	s_waitcnt vmcnt(16)
	v_lshlrev_b32_e32 v2, 16, v232
	v_and_b32_e32 v3, 0xffff0000, v232
	v_mul_f32_e32 v2, v67, v2
	v_mul_f32_e32 v3, v67, v3
	v_mul_f32_e32 v2, v200, v2
	v_mul_f32_e32 v3, v201, v3
	v_cvt_pk_fp8_f32 v10, v2, v3
	v_lshlrev_b32_e32 v4, 16, v233
	v_and_b32_e32 v5, 0xffff0000, v233
	v_mul_f32_e32 v4, v67, v4
	v_mul_f32_e32 v5, v67, v5
	v_mul_f32_e32 v4, v202, v4
	v_mul_f32_e32 v5, v203, v5
	v_cvt_pk_fp8_f32 v10, v4, v5 op_sel:[0,0,1]
	global_store_dword v[8:9], v10, off
	v_lshlrev_b32_e32 v2, 16, v234
	v_and_b32_e32 v3, 0xffff0000, v234
	v_mul_f32_e32 v2, v67, v2
	v_mul_f32_e32 v3, v67, v3
	v_mul_f32_e32 v2, v204, v2
	v_mul_f32_e32 v3, v205, v3
	v_cvt_pk_fp8_f32 v12, v2, v3
	v_lshlrev_b32_e32 v4, 16, v235
	v_and_b32_e32 v5, 0xffff0000, v235
	v_mul_f32_e32 v4, v67, v4
	v_mul_f32_e32 v5, v67, v5
	v_mul_f32_e32 v4, v206, v4
	v_mul_f32_e32 v5, v207, v5
	v_cvt_pk_fp8_f32 v12, v4, v5 op_sel:[0,0,1]
	global_store_dword v[8:9], v12, off offset:256
	v_lshlrev_b32_e32 v2, 16, v236
	v_and_b32_e32 v3, 0xffff0000, v236
	v_mul_f32_e32 v2, v67, v2
	v_mul_f32_e32 v3, v67, v3
	v_mul_f32_e32 v2, v208, v2
	v_mul_f32_e32 v3, v209, v3
	v_cvt_pk_fp8_f32 v10, v2, v3
	v_lshlrev_b32_e32 v4, 16, v237
	v_and_b32_e32 v5, 0xffff0000, v237
	v_mul_f32_e32 v4, v67, v4
	v_mul_f32_e32 v5, v67, v5
	v_mul_f32_e32 v4, v210, v4
	v_mul_f32_e32 v5, v211, v5
	v_cvt_pk_fp8_f32 v10, v4, v5 op_sel:[0,0,1]
	global_store_dword v[8:9], v10, off offset:512
	v_lshlrev_b32_e32 v2, 16, v238
	v_and_b32_e32 v3, 0xffff0000, v238
	v_mul_f32_e32 v2, v67, v2
	v_mul_f32_e32 v3, v67, v3
	v_mul_f32_e32 v2, v212, v2
	v_mul_f32_e32 v3, v213, v3
	v_cvt_pk_fp8_f32 v12, v2, v3
	v_lshlrev_b32_e32 v4, 16, v239
	v_and_b32_e32 v5, 0xffff0000, v239
	v_mul_f32_e32 v4, v67, v4
	v_mul_f32_e32 v5, v67, v5
	v_mul_f32_e32 v4, v214, v4
	v_mul_f32_e32 v5, v215, v5
	v_cvt_pk_fp8_f32 v12, v4, v5 op_sel:[0,0,1]
	global_store_dword v[8:9], v12, off offset:768
	v_lshlrev_b32_e32 v2, 16, v240
	v_and_b32_e32 v3, 0xffff0000, v240
	v_mul_f32_e32 v2, v67, v2
	v_mul_f32_e32 v3, v67, v3
	v_mul_f32_e32 v2, v216, v2
	v_mul_f32_e32 v3, v217, v3
	v_cvt_pk_fp8_f32 v10, v2, v3
	v_lshlrev_b32_e32 v4, 16, v241
	v_and_b32_e32 v5, 0xffff0000, v241
	v_mul_f32_e32 v4, v67, v4
	v_mul_f32_e32 v5, v67, v5
	v_mul_f32_e32 v4, v218, v4
	v_mul_f32_e32 v5, v219, v5
	v_cvt_pk_fp8_f32 v10, v4, v5 op_sel:[0,0,1]
	global_store_dword v[8:9], v10, off offset:1024
	v_lshlrev_b32_e32 v2, 16, v242
	v_and_b32_e32 v3, 0xffff0000, v242
	v_mul_f32_e32 v2, v67, v2
	v_mul_f32_e32 v3, v67, v3
	v_mul_f32_e32 v2, v220, v2
	v_mul_f32_e32 v3, v221, v3
	v_cvt_pk_fp8_f32 v12, v2, v3
	v_lshlrev_b32_e32 v4, 16, v243
	v_and_b32_e32 v5, 0xffff0000, v243
	v_mul_f32_e32 v4, v67, v4
	v_mul_f32_e32 v5, v67, v5
	v_mul_f32_e32 v4, v222, v4
	v_mul_f32_e32 v5, v223, v5
	v_cvt_pk_fp8_f32 v12, v4, v5 op_sel:[0,0,1]
	global_store_dword v[8:9], v12, off offset:1280
	v_lshlrev_b32_e32 v2, 16, v244
	v_and_b32_e32 v3, 0xffff0000, v244
	v_mul_f32_e32 v2, v67, v2
	v_mul_f32_e32 v3, v67, v3
	v_mul_f32_e32 v2, v224, v2
	v_mul_f32_e32 v3, v225, v3
	v_cvt_pk_fp8_f32 v10, v2, v3
	v_lshlrev_b32_e32 v4, 16, v245
	v_and_b32_e32 v5, 0xffff0000, v245
	v_mul_f32_e32 v4, v67, v4
	v_mul_f32_e32 v5, v67, v5
	v_mul_f32_e32 v4, v226, v4
	v_mul_f32_e32 v5, v227, v5
	v_cvt_pk_fp8_f32 v10, v4, v5 op_sel:[0,0,1]
	global_store_dword v[8:9], v10, off offset:1536
	v_lshlrev_b32_e32 v2, 16, v246
	v_and_b32_e32 v3, 0xffff0000, v246
	v_mul_f32_e32 v2, v67, v2
	v_mul_f32_e32 v3, v67, v3
	v_mul_f32_e32 v2, v228, v2
	v_mul_f32_e32 v3, v229, v3
	v_cvt_pk_fp8_f32 v12, v2, v3
	v_lshlrev_b32_e32 v4, 16, v247
	v_and_b32_e32 v5, 0xffff0000, v247
	v_mul_f32_e32 v4, v67, v4
	v_mul_f32_e32 v5, v67, v5
	v_mul_f32_e32 v4, v230, v4
	v_mul_f32_e32 v5, v231, v5
	v_cvt_pk_fp8_f32 v12, v4, v5 op_sel:[0,0,1]
	global_store_dword v[8:9], v12, off offset:1792
	s_add_i32 s10, s88, -3
	s_ashr_i32 s11, s10, 31
	s_lshl_b64 s[10:11], s[10:11], 12
	v_lshl_add_u64 v[6:7], v[48:49], 0, s[10:11]
	global_load_dwordx2 v[232:233], v[6:7], off
	global_load_dwordx2 v[234:235], v[6:7], off offset:512
	global_load_dwordx2 v[236:237], v[6:7], off offset:1024
	global_load_dwordx2 v[238:239], v[6:7], off offset:1536
	global_load_dwordx2 v[240:241], v[6:7], off offset:2048
	global_load_dwordx2 v[242:243], v[6:7], off offset:2560
	global_load_dwordx2 v[244:245], v[6:7], off offset:3072
	global_load_dwordx2 v[246:247], v[6:7], off offset:3584
	s_add_i32 s12, s88, -4
	s_ashr_i32 s13, s12, 31
	s_lshl_b64 s[12:13], s[12:13], 11
	v_lshl_add_u64 v[8:9], v[52:53], 0, s[12:13]
	s_waitcnt vmcnt(16)
	v_lshlrev_b32_e32 v2, 16, v170
	v_and_b32_e32 v3, 0xffff0000, v170
	v_mul_f32_e32 v2, v66, v2
	v_mul_f32_e32 v3, v66, v3
	v_mul_f32_e32 v2, v200, v2
	v_mul_f32_e32 v3, v201, v3
	v_cvt_pk_fp8_f32 v10, v2, v3
	v_lshlrev_b32_e32 v4, 16, v171
	v_and_b32_e32 v5, 0xffff0000, v171
	v_mul_f32_e32 v4, v66, v4
	v_mul_f32_e32 v5, v66, v5
	v_mul_f32_e32 v4, v202, v4
	v_mul_f32_e32 v5, v203, v5
	v_cvt_pk_fp8_f32 v10, v4, v5 op_sel:[0,0,1]
	global_store_dword v[8:9], v10, off
	v_lshlrev_b32_e32 v2, 16, v172
	v_and_b32_e32 v3, 0xffff0000, v172
	v_mul_f32_e32 v2, v66, v2
	v_mul_f32_e32 v3, v66, v3
	v_mul_f32_e32 v2, v204, v2
	v_mul_f32_e32 v3, v205, v3
	v_cvt_pk_fp8_f32 v12, v2, v3
	v_lshlrev_b32_e32 v4, 16, v173
	v_and_b32_e32 v5, 0xffff0000, v173
	v_mul_f32_e32 v4, v66, v4
	v_mul_f32_e32 v5, v66, v5
	v_mul_f32_e32 v4, v206, v4
	v_mul_f32_e32 v5, v207, v5
	v_cvt_pk_fp8_f32 v12, v4, v5 op_sel:[0,0,1]
	global_store_dword v[8:9], v12, off offset:256
	v_lshlrev_b32_e32 v2, 16, v174
	v_and_b32_e32 v3, 0xffff0000, v174
	v_mul_f32_e32 v2, v66, v2
	v_mul_f32_e32 v3, v66, v3
	v_mul_f32_e32 v2, v208, v2
	v_mul_f32_e32 v3, v209, v3
	v_cvt_pk_fp8_f32 v10, v2, v3
	v_lshlrev_b32_e32 v4, 16, v175
	v_and_b32_e32 v5, 0xffff0000, v175
	v_mul_f32_e32 v4, v66, v4
	v_mul_f32_e32 v5, v66, v5
	v_mul_f32_e32 v4, v210, v4
	v_mul_f32_e32 v5, v211, v5
	v_cvt_pk_fp8_f32 v10, v4, v5 op_sel:[0,0,1]
	global_store_dword v[8:9], v10, off offset:512
	v_lshlrev_b32_e32 v2, 16, v176
	v_and_b32_e32 v3, 0xffff0000, v176
	v_mul_f32_e32 v2, v66, v2
	v_mul_f32_e32 v3, v66, v3
	v_mul_f32_e32 v2, v212, v2
	v_mul_f32_e32 v3, v213, v3
	v_cvt_pk_fp8_f32 v12, v2, v3
	v_lshlrev_b32_e32 v4, 16, v177
	v_and_b32_e32 v5, 0xffff0000, v177
	v_mul_f32_e32 v4, v66, v4
	v_mul_f32_e32 v5, v66, v5
	v_mul_f32_e32 v4, v214, v4
	v_mul_f32_e32 v5, v215, v5
	v_cvt_pk_fp8_f32 v12, v4, v5 op_sel:[0,0,1]
	global_store_dword v[8:9], v12, off offset:768
	v_lshlrev_b32_e32 v2, 16, v178
	v_and_b32_e32 v3, 0xffff0000, v178
	v_mul_f32_e32 v2, v66, v2
	v_mul_f32_e32 v3, v66, v3
	v_mul_f32_e32 v2, v216, v2
	v_mul_f32_e32 v3, v217, v3
	v_cvt_pk_fp8_f32 v10, v2, v3
	v_lshlrev_b32_e32 v4, 16, v179
	v_and_b32_e32 v5, 0xffff0000, v179
	v_mul_f32_e32 v4, v66, v4
	v_mul_f32_e32 v5, v66, v5
	v_mul_f32_e32 v4, v218, v4
	v_mul_f32_e32 v5, v219, v5
	v_cvt_pk_fp8_f32 v10, v4, v5 op_sel:[0,0,1]
	global_store_dword v[8:9], v10, off offset:1024
	v_lshlrev_b32_e32 v2, 16, v180
	v_and_b32_e32 v3, 0xffff0000, v180
	v_mul_f32_e32 v2, v66, v2
	v_mul_f32_e32 v3, v66, v3
	v_mul_f32_e32 v2, v220, v2
	v_mul_f32_e32 v3, v221, v3
	v_cvt_pk_fp8_f32 v12, v2, v3
	v_lshlrev_b32_e32 v4, 16, v181
	v_and_b32_e32 v5, 0xffff0000, v181
	v_mul_f32_e32 v4, v66, v4
	v_mul_f32_e32 v5, v66, v5
	v_mul_f32_e32 v4, v222, v4
	v_mul_f32_e32 v5, v223, v5
	v_cvt_pk_fp8_f32 v12, v4, v5 op_sel:[0,0,1]
	global_store_dword v[8:9], v12, off offset:1280
	v_lshlrev_b32_e32 v2, 16, v182
	v_and_b32_e32 v3, 0xffff0000, v182
	v_mul_f32_e32 v2, v66, v2
	v_mul_f32_e32 v3, v66, v3
	v_mul_f32_e32 v2, v224, v2
	v_mul_f32_e32 v3, v225, v3
	v_cvt_pk_fp8_f32 v10, v2, v3
	v_lshlrev_b32_e32 v4, 16, v183
	v_and_b32_e32 v5, 0xffff0000, v183
	v_mul_f32_e32 v4, v66, v4
	v_mul_f32_e32 v5, v66, v5
	v_mul_f32_e32 v4, v226, v4
	v_mul_f32_e32 v5, v227, v5
	v_cvt_pk_fp8_f32 v10, v4, v5 op_sel:[0,0,1]
	global_store_dword v[8:9], v10, off offset:1536
	v_lshlrev_b32_e32 v2, 16, v184
	v_and_b32_e32 v3, 0xffff0000, v184
	v_mul_f32_e32 v2, v66, v2
	v_mul_f32_e32 v3, v66, v3
	v_mul_f32_e32 v2, v228, v2
	v_mul_f32_e32 v3, v229, v3
	v_cvt_pk_fp8_f32 v12, v2, v3
	v_lshlrev_b32_e32 v4, 16, v185
	v_and_b32_e32 v5, 0xffff0000, v185
	v_mul_f32_e32 v4, v66, v4
	v_mul_f32_e32 v5, v66, v5
	v_mul_f32_e32 v4, v230, v4
	v_mul_f32_e32 v5, v231, v5
	v_cvt_pk_fp8_f32 v12, v4, v5 op_sel:[0,0,1]
	global_store_dword v[8:9], v12, off offset:1792
	s_add_i32 s10, s88, -2
	s_ashr_i32 s11, s10, 31
	s_lshl_b64 s[10:11], s[10:11], 12
	v_lshl_add_u64 v[6:7], v[48:49], 0, s[10:11]
	global_load_dwordx2 v[170:171], v[6:7], off
	global_load_dwordx2 v[172:173], v[6:7], off offset:512
	global_load_dwordx2 v[174:175], v[6:7], off offset:1024
	global_load_dwordx2 v[176:177], v[6:7], off offset:1536
	global_load_dwordx2 v[178:179], v[6:7], off offset:2048
	global_load_dwordx2 v[180:181], v[6:7], off offset:2560
	global_load_dwordx2 v[182:183], v[6:7], off offset:3072
	global_load_dwordx2 v[184:185], v[6:7], off offset:3584
	s_add_i32 s12, s88, -3
	s_ashr_i32 s13, s12, 31
	s_lshl_b64 s[12:13], s[12:13], 11
	v_lshl_add_u64 v[8:9], v[52:53], 0, s[12:13]
	s_waitcnt vmcnt(16)
	v_lshlrev_b32_e32 v2, 16, v232
	v_and_b32_e32 v3, 0xffff0000, v232
	v_mul_f32_e32 v2, v65, v2
	v_mul_f32_e32 v3, v65, v3
	v_mul_f32_e32 v2, v200, v2
	v_mul_f32_e32 v3, v201, v3
	v_cvt_pk_fp8_f32 v10, v2, v3
	v_lshlrev_b32_e32 v4, 16, v233
	v_and_b32_e32 v5, 0xffff0000, v233
	v_mul_f32_e32 v4, v65, v4
	v_mul_f32_e32 v5, v65, v5
	v_mul_f32_e32 v4, v202, v4
	v_mul_f32_e32 v5, v203, v5
	v_cvt_pk_fp8_f32 v10, v4, v5 op_sel:[0,0,1]
	global_store_dword v[8:9], v10, off
	v_lshlrev_b32_e32 v2, 16, v234
	v_and_b32_e32 v3, 0xffff0000, v234
	v_mul_f32_e32 v2, v65, v2
	v_mul_f32_e32 v3, v65, v3
	v_mul_f32_e32 v2, v204, v2
	v_mul_f32_e32 v3, v205, v3
	v_cvt_pk_fp8_f32 v12, v2, v3
	v_lshlrev_b32_e32 v4, 16, v235
	v_and_b32_e32 v5, 0xffff0000, v235
	v_mul_f32_e32 v4, v65, v4
	v_mul_f32_e32 v5, v65, v5
	v_mul_f32_e32 v4, v206, v4
	v_mul_f32_e32 v5, v207, v5
	v_cvt_pk_fp8_f32 v12, v4, v5 op_sel:[0,0,1]
	global_store_dword v[8:9], v12, off offset:256
	v_lshlrev_b32_e32 v2, 16, v236
	v_and_b32_e32 v3, 0xffff0000, v236
	v_mul_f32_e32 v2, v65, v2
	v_mul_f32_e32 v3, v65, v3
	v_mul_f32_e32 v2, v208, v2
	v_mul_f32_e32 v3, v209, v3
	v_cvt_pk_fp8_f32 v10, v2, v3
	v_lshlrev_b32_e32 v4, 16, v237
	v_and_b32_e32 v5, 0xffff0000, v237
	v_mul_f32_e32 v4, v65, v4
	v_mul_f32_e32 v5, v65, v5
	v_mul_f32_e32 v4, v210, v4
	v_mul_f32_e32 v5, v211, v5
	v_cvt_pk_fp8_f32 v10, v4, v5 op_sel:[0,0,1]
	global_store_dword v[8:9], v10, off offset:512
	v_lshlrev_b32_e32 v2, 16, v238
	v_and_b32_e32 v3, 0xffff0000, v238
	v_mul_f32_e32 v2, v65, v2
	v_mul_f32_e32 v3, v65, v3
	v_mul_f32_e32 v2, v212, v2
	v_mul_f32_e32 v3, v213, v3
	v_cvt_pk_fp8_f32 v12, v2, v3
	v_lshlrev_b32_e32 v4, 16, v239
	v_and_b32_e32 v5, 0xffff0000, v239
	v_mul_f32_e32 v4, v65, v4
	v_mul_f32_e32 v5, v65, v5
	v_mul_f32_e32 v4, v214, v4
	v_mul_f32_e32 v5, v215, v5
	v_cvt_pk_fp8_f32 v12, v4, v5 op_sel:[0,0,1]
	global_store_dword v[8:9], v12, off offset:768
	v_lshlrev_b32_e32 v2, 16, v240
	v_and_b32_e32 v3, 0xffff0000, v240
	v_mul_f32_e32 v2, v65, v2
	v_mul_f32_e32 v3, v65, v3
	v_mul_f32_e32 v2, v216, v2
	v_mul_f32_e32 v3, v217, v3
	v_cvt_pk_fp8_f32 v10, v2, v3
	v_lshlrev_b32_e32 v4, 16, v241
	v_and_b32_e32 v5, 0xffff0000, v241
	v_mul_f32_e32 v4, v65, v4
	v_mul_f32_e32 v5, v65, v5
	v_mul_f32_e32 v4, v218, v4
	v_mul_f32_e32 v5, v219, v5
	v_cvt_pk_fp8_f32 v10, v4, v5 op_sel:[0,0,1]
	global_store_dword v[8:9], v10, off offset:1024
	v_lshlrev_b32_e32 v2, 16, v242
	v_and_b32_e32 v3, 0xffff0000, v242
	v_mul_f32_e32 v2, v65, v2
	v_mul_f32_e32 v3, v65, v3
	v_mul_f32_e32 v2, v220, v2
	v_mul_f32_e32 v3, v221, v3
	v_cvt_pk_fp8_f32 v12, v2, v3
	v_lshlrev_b32_e32 v4, 16, v243
	v_and_b32_e32 v5, 0xffff0000, v243
	v_mul_f32_e32 v4, v65, v4
	v_mul_f32_e32 v5, v65, v5
	v_mul_f32_e32 v4, v222, v4
	v_mul_f32_e32 v5, v223, v5
	v_cvt_pk_fp8_f32 v12, v4, v5 op_sel:[0,0,1]
	global_store_dword v[8:9], v12, off offset:1280
	v_lshlrev_b32_e32 v2, 16, v244
	v_and_b32_e32 v3, 0xffff0000, v244
	v_mul_f32_e32 v2, v65, v2
	v_mul_f32_e32 v3, v65, v3
	v_mul_f32_e32 v2, v224, v2
	v_mul_f32_e32 v3, v225, v3
	v_cvt_pk_fp8_f32 v10, v2, v3
	v_lshlrev_b32_e32 v4, 16, v245
	v_and_b32_e32 v5, 0xffff0000, v245
	v_mul_f32_e32 v4, v65, v4
	v_mul_f32_e32 v5, v65, v5
	v_mul_f32_e32 v4, v226, v4
	v_mul_f32_e32 v5, v227, v5
	v_cvt_pk_fp8_f32 v10, v4, v5 op_sel:[0,0,1]
	global_store_dword v[8:9], v10, off offset:1536
	v_lshlrev_b32_e32 v2, 16, v246
	v_and_b32_e32 v3, 0xffff0000, v246
	v_mul_f32_e32 v2, v65, v2
	v_mul_f32_e32 v3, v65, v3
	v_mul_f32_e32 v2, v228, v2
	v_mul_f32_e32 v3, v229, v3
	v_cvt_pk_fp8_f32 v12, v2, v3
	v_lshlrev_b32_e32 v4, 16, v247
	v_and_b32_e32 v5, 0xffff0000, v247
	v_mul_f32_e32 v4, v65, v4
	v_mul_f32_e32 v5, v65, v5
	v_mul_f32_e32 v4, v230, v4
	v_mul_f32_e32 v5, v231, v5
	v_cvt_pk_fp8_f32 v12, v4, v5 op_sel:[0,0,1]
	global_store_dword v[8:9], v12, off offset:1792
	s_add_i32 s10, s88, -1
	s_ashr_i32 s11, s10, 31
	s_lshl_b64 s[10:11], s[10:11], 12
	v_lshl_add_u64 v[6:7], v[48:49], 0, s[10:11]
	global_load_dwordx2 v[232:233], v[6:7], off
	global_load_dwordx2 v[234:235], v[6:7], off offset:512
	global_load_dwordx2 v[236:237], v[6:7], off offset:1024
	global_load_dwordx2 v[238:239], v[6:7], off offset:1536
	global_load_dwordx2 v[240:241], v[6:7], off offset:2048
	global_load_dwordx2 v[242:243], v[6:7], off offset:2560
	global_load_dwordx2 v[244:245], v[6:7], off offset:3072
	global_load_dwordx2 v[246:247], v[6:7], off offset:3584
	s_add_i32 s12, s88, -2
	s_ashr_i32 s13, s12, 31
	s_lshl_b64 s[12:13], s[12:13], 11
	v_lshl_add_u64 v[8:9], v[52:53], 0, s[12:13]
	s_waitcnt vmcnt(16)
	v_lshlrev_b32_e32 v2, 16, v170
	v_and_b32_e32 v3, 0xffff0000, v170
	v_mul_f32_e32 v2, v64, v2
	v_mul_f32_e32 v3, v64, v3
	v_mul_f32_e32 v2, v200, v2
	v_mul_f32_e32 v3, v201, v3
	v_cvt_pk_fp8_f32 v10, v2, v3
	v_lshlrev_b32_e32 v4, 16, v171
	v_and_b32_e32 v5, 0xffff0000, v171
	v_mul_f32_e32 v4, v64, v4
	v_mul_f32_e32 v5, v64, v5
	v_mul_f32_e32 v4, v202, v4
	v_mul_f32_e32 v5, v203, v5
	v_cvt_pk_fp8_f32 v10, v4, v5 op_sel:[0,0,1]
	global_store_dword v[8:9], v10, off
	v_lshlrev_b32_e32 v2, 16, v172
	v_and_b32_e32 v3, 0xffff0000, v172
	v_mul_f32_e32 v2, v64, v2
	v_mul_f32_e32 v3, v64, v3
	v_mul_f32_e32 v2, v204, v2
	v_mul_f32_e32 v3, v205, v3
	v_cvt_pk_fp8_f32 v12, v2, v3
	v_lshlrev_b32_e32 v4, 16, v173
	v_and_b32_e32 v5, 0xffff0000, v173
	v_mul_f32_e32 v4, v64, v4
	v_mul_f32_e32 v5, v64, v5
	v_mul_f32_e32 v4, v206, v4
	v_mul_f32_e32 v5, v207, v5
	v_cvt_pk_fp8_f32 v12, v4, v5 op_sel:[0,0,1]
	global_store_dword v[8:9], v12, off offset:256
	v_lshlrev_b32_e32 v2, 16, v174
	v_and_b32_e32 v3, 0xffff0000, v174
	v_mul_f32_e32 v2, v64, v2
	v_mul_f32_e32 v3, v64, v3
	v_mul_f32_e32 v2, v208, v2
	v_mul_f32_e32 v3, v209, v3
	v_cvt_pk_fp8_f32 v10, v2, v3
	v_lshlrev_b32_e32 v4, 16, v175
	v_and_b32_e32 v5, 0xffff0000, v175
	v_mul_f32_e32 v4, v64, v4
	v_mul_f32_e32 v5, v64, v5
	v_mul_f32_e32 v4, v210, v4
	v_mul_f32_e32 v5, v211, v5
	v_cvt_pk_fp8_f32 v10, v4, v5 op_sel:[0,0,1]
	global_store_dword v[8:9], v10, off offset:512
	v_lshlrev_b32_e32 v2, 16, v176
	v_and_b32_e32 v3, 0xffff0000, v176
	v_mul_f32_e32 v2, v64, v2
	v_mul_f32_e32 v3, v64, v3
	v_mul_f32_e32 v2, v212, v2
	v_mul_f32_e32 v3, v213, v3
	v_cvt_pk_fp8_f32 v12, v2, v3
	v_lshlrev_b32_e32 v4, 16, v177
	v_and_b32_e32 v5, 0xffff0000, v177
	v_mul_f32_e32 v4, v64, v4
	v_mul_f32_e32 v5, v64, v5
	v_mul_f32_e32 v4, v214, v4
	v_mul_f32_e32 v5, v215, v5
	v_cvt_pk_fp8_f32 v12, v4, v5 op_sel:[0,0,1]
	global_store_dword v[8:9], v12, off offset:768
	v_lshlrev_b32_e32 v2, 16, v178
	v_and_b32_e32 v3, 0xffff0000, v178
	v_mul_f32_e32 v2, v64, v2
	v_mul_f32_e32 v3, v64, v3
	v_mul_f32_e32 v2, v216, v2
	v_mul_f32_e32 v3, v217, v3
	v_cvt_pk_fp8_f32 v10, v2, v3
	v_lshlrev_b32_e32 v4, 16, v179
	v_and_b32_e32 v5, 0xffff0000, v179
	v_mul_f32_e32 v4, v64, v4
	v_mul_f32_e32 v5, v64, v5
	v_mul_f32_e32 v4, v218, v4
	v_mul_f32_e32 v5, v219, v5
	v_cvt_pk_fp8_f32 v10, v4, v5 op_sel:[0,0,1]
	global_store_dword v[8:9], v10, off offset:1024
	v_lshlrev_b32_e32 v2, 16, v180
	v_and_b32_e32 v3, 0xffff0000, v180
	v_mul_f32_e32 v2, v64, v2
	v_mul_f32_e32 v3, v64, v3
	v_mul_f32_e32 v2, v220, v2
	v_mul_f32_e32 v3, v221, v3
	v_cvt_pk_fp8_f32 v12, v2, v3
	v_lshlrev_b32_e32 v4, 16, v181
	v_and_b32_e32 v5, 0xffff0000, v181
	v_mul_f32_e32 v4, v64, v4
	v_mul_f32_e32 v5, v64, v5
	v_mul_f32_e32 v4, v222, v4
	v_mul_f32_e32 v5, v223, v5
	v_cvt_pk_fp8_f32 v12, v4, v5 op_sel:[0,0,1]
	global_store_dword v[8:9], v12, off offset:1280
	v_lshlrev_b32_e32 v2, 16, v182
	v_and_b32_e32 v3, 0xffff0000, v182
	v_mul_f32_e32 v2, v64, v2
	v_mul_f32_e32 v3, v64, v3
	v_mul_f32_e32 v2, v224, v2
	v_mul_f32_e32 v3, v225, v3
	v_cvt_pk_fp8_f32 v10, v2, v3
	v_lshlrev_b32_e32 v4, 16, v183
	v_and_b32_e32 v5, 0xffff0000, v183
	v_mul_f32_e32 v4, v64, v4
	v_mul_f32_e32 v5, v64, v5
	v_mul_f32_e32 v4, v226, v4
	v_mul_f32_e32 v5, v227, v5
	v_cvt_pk_fp8_f32 v10, v4, v5 op_sel:[0,0,1]
	global_store_dword v[8:9], v10, off offset:1536
	v_lshlrev_b32_e32 v2, 16, v184
	v_and_b32_e32 v3, 0xffff0000, v184
	v_mul_f32_e32 v2, v64, v2
	v_mul_f32_e32 v3, v64, v3
	v_mul_f32_e32 v2, v228, v2
	v_mul_f32_e32 v3, v229, v3
	v_cvt_pk_fp8_f32 v12, v2, v3
	v_lshlrev_b32_e32 v4, 16, v185
	v_and_b32_e32 v5, 0xffff0000, v185
	v_mul_f32_e32 v4, v64, v4
	v_mul_f32_e32 v5, v64, v5
	v_mul_f32_e32 v4, v230, v4
	v_mul_f32_e32 v5, v231, v5
	v_cvt_pk_fp8_f32 v12, v4, v5 op_sel:[0,0,1]
	global_store_dword v[8:9], v12, off offset:1792
	s_mov_b64 s[10:11], s[88:89]
	s_lshl_b64 s[10:11], s[10:11], 12
	v_lshl_add_u64 v[6:7], v[48:49], 0, s[10:11]
	global_load_dwordx2 v[170:171], v[6:7], off
	global_load_dwordx2 v[172:173], v[6:7], off offset:512
	global_load_dwordx2 v[174:175], v[6:7], off offset:1024
	global_load_dwordx2 v[176:177], v[6:7], off offset:1536
	global_load_dwordx2 v[178:179], v[6:7], off offset:2048
	global_load_dwordx2 v[180:181], v[6:7], off offset:2560
	global_load_dwordx2 v[182:183], v[6:7], off offset:3072
	global_load_dwordx2 v[184:185], v[6:7], off offset:3584
	s_add_i32 s12, s88, -1
	s_ashr_i32 s13, s12, 31
	s_lshl_b64 s[12:13], s[12:13], 11
	v_lshl_add_u64 v[8:9], v[52:53], 0, s[12:13]
	s_waitcnt vmcnt(16)
	v_lshlrev_b32_e32 v2, 16, v232
	v_and_b32_e32 v3, 0xffff0000, v232
	v_mul_f32_e32 v2, v63, v2
	v_mul_f32_e32 v3, v63, v3
	v_mul_f32_e32 v2, v200, v2
	v_mul_f32_e32 v3, v201, v3
	v_cvt_pk_fp8_f32 v10, v2, v3
	v_lshlrev_b32_e32 v4, 16, v233
	v_and_b32_e32 v5, 0xffff0000, v233
	v_mul_f32_e32 v4, v63, v4
	v_mul_f32_e32 v5, v63, v5
	v_mul_f32_e32 v4, v202, v4
	v_mul_f32_e32 v5, v203, v5
	v_cvt_pk_fp8_f32 v10, v4, v5 op_sel:[0,0,1]
	global_store_dword v[8:9], v10, off
	v_lshlrev_b32_e32 v2, 16, v234
	v_and_b32_e32 v3, 0xffff0000, v234
	v_mul_f32_e32 v2, v63, v2
	v_mul_f32_e32 v3, v63, v3
	v_mul_f32_e32 v2, v204, v2
	v_mul_f32_e32 v3, v205, v3
	v_cvt_pk_fp8_f32 v12, v2, v3
	v_lshlrev_b32_e32 v4, 16, v235
	v_and_b32_e32 v5, 0xffff0000, v235
	v_mul_f32_e32 v4, v63, v4
	v_mul_f32_e32 v5, v63, v5
	v_mul_f32_e32 v4, v206, v4
	v_mul_f32_e32 v5, v207, v5
	v_cvt_pk_fp8_f32 v12, v4, v5 op_sel:[0,0,1]
	global_store_dword v[8:9], v12, off offset:256
	v_lshlrev_b32_e32 v2, 16, v236
	v_and_b32_e32 v3, 0xffff0000, v236
	v_mul_f32_e32 v2, v63, v2
	v_mul_f32_e32 v3, v63, v3
	v_mul_f32_e32 v2, v208, v2
	v_mul_f32_e32 v3, v209, v3
	v_cvt_pk_fp8_f32 v10, v2, v3
	v_lshlrev_b32_e32 v4, 16, v237
	v_and_b32_e32 v5, 0xffff0000, v237
	v_mul_f32_e32 v4, v63, v4
	v_mul_f32_e32 v5, v63, v5
	v_mul_f32_e32 v4, v210, v4
	v_mul_f32_e32 v5, v211, v5
	v_cvt_pk_fp8_f32 v10, v4, v5 op_sel:[0,0,1]
	global_store_dword v[8:9], v10, off offset:512
	v_lshlrev_b32_e32 v2, 16, v238
	v_and_b32_e32 v3, 0xffff0000, v238
	v_mul_f32_e32 v2, v63, v2
	v_mul_f32_e32 v3, v63, v3
	v_mul_f32_e32 v2, v212, v2
	v_mul_f32_e32 v3, v213, v3
	v_cvt_pk_fp8_f32 v12, v2, v3
	v_lshlrev_b32_e32 v4, 16, v239
	v_and_b32_e32 v5, 0xffff0000, v239
	v_mul_f32_e32 v4, v63, v4
	v_mul_f32_e32 v5, v63, v5
	v_mul_f32_e32 v4, v214, v4
	v_mul_f32_e32 v5, v215, v5
	v_cvt_pk_fp8_f32 v12, v4, v5 op_sel:[0,0,1]
	global_store_dword v[8:9], v12, off offset:768
	v_lshlrev_b32_e32 v2, 16, v240
	v_and_b32_e32 v3, 0xffff0000, v240
	v_mul_f32_e32 v2, v63, v2
	v_mul_f32_e32 v3, v63, v3
	v_mul_f32_e32 v2, v216, v2
	v_mul_f32_e32 v3, v217, v3
	v_cvt_pk_fp8_f32 v10, v2, v3
	v_lshlrev_b32_e32 v4, 16, v241
	v_and_b32_e32 v5, 0xffff0000, v241
	v_mul_f32_e32 v4, v63, v4
	v_mul_f32_e32 v5, v63, v5
	v_mul_f32_e32 v4, v218, v4
	v_mul_f32_e32 v5, v219, v5
	v_cvt_pk_fp8_f32 v10, v4, v5 op_sel:[0,0,1]
	global_store_dword v[8:9], v10, off offset:1024
	v_lshlrev_b32_e32 v2, 16, v242
	v_and_b32_e32 v3, 0xffff0000, v242
	v_mul_f32_e32 v2, v63, v2
	v_mul_f32_e32 v3, v63, v3
	v_mul_f32_e32 v2, v220, v2
	v_mul_f32_e32 v3, v221, v3
	v_cvt_pk_fp8_f32 v12, v2, v3
	v_lshlrev_b32_e32 v4, 16, v243
	v_and_b32_e32 v5, 0xffff0000, v243
	v_mul_f32_e32 v4, v63, v4
	v_mul_f32_e32 v5, v63, v5
	v_mul_f32_e32 v4, v222, v4
	v_mul_f32_e32 v5, v223, v5
	v_cvt_pk_fp8_f32 v12, v4, v5 op_sel:[0,0,1]
	global_store_dword v[8:9], v12, off offset:1280
	v_lshlrev_b32_e32 v2, 16, v244
	v_and_b32_e32 v3, 0xffff0000, v244
	v_mul_f32_e32 v2, v63, v2
	v_mul_f32_e32 v3, v63, v3
	v_mul_f32_e32 v2, v224, v2
	v_mul_f32_e32 v3, v225, v3
	v_cvt_pk_fp8_f32 v10, v2, v3
	v_lshlrev_b32_e32 v4, 16, v245
	v_and_b32_e32 v5, 0xffff0000, v245
	v_mul_f32_e32 v4, v63, v4
	v_mul_f32_e32 v5, v63, v5
	v_mul_f32_e32 v4, v226, v4
	v_mul_f32_e32 v5, v227, v5
	v_cvt_pk_fp8_f32 v10, v4, v5 op_sel:[0,0,1]
	global_store_dword v[8:9], v10, off offset:1536
	v_lshlrev_b32_e32 v2, 16, v246
	v_and_b32_e32 v3, 0xffff0000, v246
	v_mul_f32_e32 v2, v63, v2
	v_mul_f32_e32 v3, v63, v3
	v_mul_f32_e32 v2, v228, v2
	v_mul_f32_e32 v3, v229, v3
	v_cvt_pk_fp8_f32 v12, v2, v3
	v_lshlrev_b32_e32 v4, 16, v247
	v_and_b32_e32 v5, 0xffff0000, v247
	v_mul_f32_e32 v4, v63, v4
	v_mul_f32_e32 v5, v63, v5
	v_mul_f32_e32 v4, v230, v4
	v_mul_f32_e32 v5, v231, v5
	v_cvt_pk_fp8_f32 v12, v4, v5 op_sel:[0,0,1]
	global_store_dword v[8:9], v12, off offset:1792
	s_mov_b64 s[12:13], s[88:89]
	s_lshl_b64 s[12:13], s[12:13], 11
	v_lshl_add_u64 v[8:9], v[52:53], 0, s[12:13]
	s_waitcnt vmcnt(8)
	v_lshlrev_b32_e32 v2, 16, v170
	v_and_b32_e32 v3, 0xffff0000, v170
	v_mul_f32_e32 v2, v62, v2
	v_mul_f32_e32 v3, v62, v3
	v_mul_f32_e32 v2, v200, v2
	v_mul_f32_e32 v3, v201, v3
	v_cvt_pk_fp8_f32 v10, v2, v3
	v_lshlrev_b32_e32 v4, 16, v171
	v_and_b32_e32 v5, 0xffff0000, v171
	v_mul_f32_e32 v4, v62, v4
	v_mul_f32_e32 v5, v62, v5
	v_mul_f32_e32 v4, v202, v4
	v_mul_f32_e32 v5, v203, v5
	v_cvt_pk_fp8_f32 v10, v4, v5 op_sel:[0,0,1]
	global_store_dword v[8:9], v10, off
	v_lshlrev_b32_e32 v2, 16, v172
	v_and_b32_e32 v3, 0xffff0000, v172
	v_mul_f32_e32 v2, v62, v2
	v_mul_f32_e32 v3, v62, v3
	v_mul_f32_e32 v2, v204, v2
	v_mul_f32_e32 v3, v205, v3
	v_cvt_pk_fp8_f32 v12, v2, v3
	v_lshlrev_b32_e32 v4, 16, v173
	v_and_b32_e32 v5, 0xffff0000, v173
	v_mul_f32_e32 v4, v62, v4
	v_mul_f32_e32 v5, v62, v5
	v_mul_f32_e32 v4, v206, v4
	v_mul_f32_e32 v5, v207, v5
	v_cvt_pk_fp8_f32 v12, v4, v5 op_sel:[0,0,1]
	global_store_dword v[8:9], v12, off offset:256
	v_lshlrev_b32_e32 v2, 16, v174
	v_and_b32_e32 v3, 0xffff0000, v174
	v_mul_f32_e32 v2, v62, v2
	v_mul_f32_e32 v3, v62, v3
	v_mul_f32_e32 v2, v208, v2
	v_mul_f32_e32 v3, v209, v3
	v_cvt_pk_fp8_f32 v10, v2, v3
	v_lshlrev_b32_e32 v4, 16, v175
	v_and_b32_e32 v5, 0xffff0000, v175
	v_mul_f32_e32 v4, v62, v4
	v_mul_f32_e32 v5, v62, v5
	v_mul_f32_e32 v4, v210, v4
	v_mul_f32_e32 v5, v211, v5
	v_cvt_pk_fp8_f32 v10, v4, v5 op_sel:[0,0,1]
	global_store_dword v[8:9], v10, off offset:512
	v_lshlrev_b32_e32 v2, 16, v176
	v_and_b32_e32 v3, 0xffff0000, v176
	v_mul_f32_e32 v2, v62, v2
	v_mul_f32_e32 v3, v62, v3
	v_mul_f32_e32 v2, v212, v2
	v_mul_f32_e32 v3, v213, v3
	v_cvt_pk_fp8_f32 v12, v2, v3
	v_lshlrev_b32_e32 v4, 16, v177
	v_and_b32_e32 v5, 0xffff0000, v177
	v_mul_f32_e32 v4, v62, v4
	v_mul_f32_e32 v5, v62, v5
	v_mul_f32_e32 v4, v214, v4
	v_mul_f32_e32 v5, v215, v5
	v_cvt_pk_fp8_f32 v12, v4, v5 op_sel:[0,0,1]
	global_store_dword v[8:9], v12, off offset:768
	v_lshlrev_b32_e32 v2, 16, v178
	v_and_b32_e32 v3, 0xffff0000, v178
	v_mul_f32_e32 v2, v62, v2
	v_mul_f32_e32 v3, v62, v3
	v_mul_f32_e32 v2, v216, v2
	v_mul_f32_e32 v3, v217, v3
	v_cvt_pk_fp8_f32 v10, v2, v3
	v_lshlrev_b32_e32 v4, 16, v179
	v_and_b32_e32 v5, 0xffff0000, v179
	v_mul_f32_e32 v4, v62, v4
	v_mul_f32_e32 v5, v62, v5
	v_mul_f32_e32 v4, v218, v4
	v_mul_f32_e32 v5, v219, v5
	v_cvt_pk_fp8_f32 v10, v4, v5 op_sel:[0,0,1]
	global_store_dword v[8:9], v10, off offset:1024
	v_lshlrev_b32_e32 v2, 16, v180
	v_and_b32_e32 v3, 0xffff0000, v180
	v_mul_f32_e32 v2, v62, v2
	v_mul_f32_e32 v3, v62, v3
	v_mul_f32_e32 v2, v220, v2
	v_mul_f32_e32 v3, v221, v3
	v_cvt_pk_fp8_f32 v12, v2, v3
	v_lshlrev_b32_e32 v4, 16, v181
	v_and_b32_e32 v5, 0xffff0000, v181
	v_mul_f32_e32 v4, v62, v4
	v_mul_f32_e32 v5, v62, v5
	v_mul_f32_e32 v4, v222, v4
	v_mul_f32_e32 v5, v223, v5
	v_cvt_pk_fp8_f32 v12, v4, v5 op_sel:[0,0,1]
	global_store_dword v[8:9], v12, off offset:1280
	v_lshlrev_b32_e32 v2, 16, v182
	v_and_b32_e32 v3, 0xffff0000, v182
	v_mul_f32_e32 v2, v62, v2
	v_mul_f32_e32 v3, v62, v3
	v_mul_f32_e32 v2, v224, v2
	v_mul_f32_e32 v3, v225, v3
	v_cvt_pk_fp8_f32 v10, v2, v3
	v_lshlrev_b32_e32 v4, 16, v183
	v_and_b32_e32 v5, 0xffff0000, v183
	v_mul_f32_e32 v4, v62, v4
	v_mul_f32_e32 v5, v62, v5
	v_mul_f32_e32 v4, v226, v4
	v_mul_f32_e32 v5, v227, v5
	v_cvt_pk_fp8_f32 v10, v4, v5 op_sel:[0,0,1]
	global_store_dword v[8:9], v10, off offset:1536
	v_lshlrev_b32_e32 v2, 16, v184
	v_and_b32_e32 v3, 0xffff0000, v184
	v_mul_f32_e32 v2, v62, v2
	v_mul_f32_e32 v3, v62, v3
	v_mul_f32_e32 v2, v228, v2
	v_mul_f32_e32 v3, v229, v3
	v_cvt_pk_fp8_f32 v12, v2, v3
	v_lshlrev_b32_e32 v4, 16, v185
	v_and_b32_e32 v5, 0xffff0000, v185
	v_mul_f32_e32 v4, v62, v4
	v_mul_f32_e32 v5, v62, v5
	v_mul_f32_e32 v4, v230, v4
	v_mul_f32_e32 v5, v231, v5
	v_cvt_pk_fp8_f32 v12, v4, v5 op_sel:[0,0,1]
	global_store_dword v[8:9], v12, off offset:1792
